# W_out fused epilogue pass 1: residual tiles staged through LDS with LDS-DMA (4 row groups ahead for f32, all 8 for bf16) instead of one serialized load round trip per row group
# speedup vs baseline: 1.0016x; 1.0001x over previous
; #define LAS __attribute__((address_space(3)))
; __device__ __forceinline__ float bflo(unsigned u) { return __uint_as_float(u << 16); }
; __device__ __forceinline__ float bfhi(unsigned u) { return __uint_as_float(u & 0xffff0000u); }
;     __device__ __forceinline__ void fused(AccT& acc, const GUnit& u, int wr, int wc, int fr, int fq, LAS unsigned char* lds, int wid, int lane) const {
;         const int b = u.pm >> 3, tid = wid * 64 + lane;
;         const int col0 = u.pn * 256 + wc * 32 + 8 * fq;
;         LAS float* P = (LAS float*)lds;
;         LAS float* S = (LAS float*)(lds + 4096);
;         LAS float* LP = (LAS float*)(lds + 8192);
;         f32x4 G[2][2];
; #pragma unroll
;         for (int bj = 0; bj < 2; ++bj)
; #pragma unroll
;             for (int n = 0; n < 2; ++n) { const int c = col0 + bj * 128 + n * 4; G[bj][n] = *(const f32x4*)(g2 + c) * (*(const f32x4*)(shf + (size_t)b * 12288 + 2048 + c) + 1.f); }
;         bf16x8 wf[2];
; #pragma unroll
;         for (int bj = 0; bj < 2; ++bj) wf[bj] = *(const bf16x8*)(WRT + (size_t)fr * 2048 + col0 + bj * 128);
;         {
;             f32x4 g[2][2];
; #pragma unroll
;             for (int bj = 0; bj < 2; ++bj)
; #pragma unroll
;                 for (int n = 0; n < 2; ++n) g[bj][n] = *(const f32x4*)(gate + (size_t)b * 12288 + col0 + bj * 128 + n * 4);
; #pragma unroll
;             for (int ai = 0; ai < 2; ++ai)
; #pragma unroll
;                 for (int m = 0; m < 4; ++m) {
;                     const size_t ro = (size_t)(u.pm * 256 + ai * 128 + wr * 64 + m * 16 + fr) * DM + col0;
; #pragma unroll
;                     for (int bj = 0; bj < 2; ++bj) {
;                         f32x4 x0, x1;
;                         if (base32) { x0 = *(const f32x4*)(base32 + ro + bj * 128); x1 = *(const f32x4*)(base32 + ro + bj * 128 + 4); }
;                         else { const u32x4 w = *(const u32x4*)(base16 + ro + bj * 128); x0 = (f32x4){bflo(w.x), bfhi(w.x), bflo(w.y), bfhi(w.y)}; x1 = (f32x4){bflo(w.z), bfhi(w.z), bflo(w.w), bfhi(w.w)}; }
.LBB0_1189:
	v_readlane_b32 s28, v250, 59
	v_readlane_b32 s29, v250, 60
	v_readlane_b32 s68, v249, 29
	s_lshl_b32 s33, s59, 5
	s_lshl_b64 s[48:49], s[28:29], 13
	v_readlane_b32 s80, v249, 41
	v_readlane_b32 s81, v249, 42
	s_add_u32 s12, s80, s48
	s_addc_u32 s13, s81, s49
	s_lshl_b64 s[28:29], s[28:29], 16
	v_readlane_b32 s34, v249, 55
	v_readlane_b32 s35, v249, 56
	s_add_u32 s28, s34, s28
	s_addc_u32 s29, s35, s29
	v_readlane_b32 s34, v255, 18
	s_mov_b32 s0, s34
	s_ashr_i32 s44, s34, 3
	v_readlane_b32 s34, v255, 17
	s_lshl_b32 s34, s34, 8
	v_bfe_u32 v208, v207, 4, 2
	s_or_b32 s33, s34, s33
	s_mul_i32 s45, s44, 0xc000
	v_lshl_or_b32 v196, v208, 3, s33
	s_mul_hi_i32 s33, s44, 0xc000
	s_add_u32 s11, s11, s45
	s_addc_u32 s22, s22, s33
	s_add_u32 s50, s11, 0x6000
	s_addc_u32 s51, s22, 0
	v_readlane_b32 s35, v255, 19
	s_add_u32 s34, s11, 0x8000
	v_ashrrev_i32_e32 v197, 31, v196
	s_addc_u32 s35, s22, 0
	v_lshlrev_b64 v[78:79], 2, v[196:197]
	v_lshl_add_u64 v[2:3], s[12:13], 0, v[78:79]
	v_lshl_add_u64 v[4:5], s[34:35], 0, v[78:79]
	s_waitcnt vmcnt(0)
	s_barrier
	global_load_dwordx4 v[94:97], v[2:3], off offset:16
	global_load_dwordx4 v[114:117], v[2:3], off
	global_load_dwordx4 v[106:109], v[4:5], off offset:16
	global_load_dwordx4 v[118:121], v[4:5], off
	v_or_b32_e32 v4, 0x80, v196
	v_ashrrev_i32_e32 v5, 31, v4
	global_load_dwordx4 v[82:85], v[2:3], off offset:528
	global_load_dwordx4 v[102:105], v[2:3], off offset:512
	v_lshl_add_u64 v[2:3], v[4:5], 2, s[34:35]
	v_lshlrev_b32_e32 v194, 12, v206
	s_add_u32 s12, s9, s45
	global_load_dwordx4 v[90:93], v[2:3], off offset:16
	global_load_dwordx4 v[110:113], v[2:3], off
	v_lshl_add_u64 v[2:3], s[28:29], 0, v[194:195]
	s_addc_u32 s13, s10, s33
	v_lshl_add_u64 v[2:3], v[196:197], 1, v[2:3]
	v_lshl_add_u64 v[98:99], s[12:13], 0, v[78:79]
	global_load_dwordx4 v[6:9], v[2:3], off
	s_nop 0
	global_load_dwordx4 v[2:5], v[2:3], off offset:256
	s_nop 0
	global_load_dwordx4 v[130:133], v[98:99], off offset:16
	global_load_dwordx4 v[134:137], v[98:99], off
	global_load_dwordx4 v[78:81], v[98:99], off offset:528
	s_nop 0
	global_load_dwordx4 v[98:101], v[98:99], off offset:512
	s_lshl_b32 s9, s0, 8
	s_add_i32 s10, s9, s23
	v_or_b32_e32 v198, s10, v206
	v_ashrrev_i32_e32 v199, 31, v198
	v_lshlrev_b64 v[186:187], 11, v[198:199]
	v_lshl_add_u64 v[204:205], v[186:187], 0, v[196:197]
	v_cndmask_b32_e64 v186, 0, 1, s[42:43]
	v_cmp_ne_u32_e64 s[34:35], 1, v186
	s_andn2_b64 vcc, exec, s[42:43]
	v_lshl_add_u64 v[200:201], v[204:205], 2, s[40:41]
	v_readlane_b32 s69, v249, 30
	v_readlane_b32 s70, v249, 31
	v_readlane_b32 s71, v249, 32
	v_readlane_b32 s72, v249, 33
	v_readlane_b32 s73, v249, 34
	v_readlane_b32 s74, v249, 35
	v_readlane_b32 s75, v249, 36
	v_readlane_b32 s76, v249, 37
	v_readlane_b32 s77, v249, 38
	v_readlane_b32 s78, v249, 39
	v_readlane_b32 s79, v249, 40
	v_readlane_b32 s82, v249, 43
	v_readlane_b32 s83, v249, 44
	s_cbranch_vccnz .LBB0_1191
	v_readfirstlane_b32 s96, v0
	v_and_b32_e32 v238, 63, v0
	v_lshlrev_b32_e32 v238, 4, v238
	s_nop 1
	s_lshr_b32 s96, s96, 6
	s_mul_i32 s96, s96, 16384
	s_addk_i32 s96, 1024
	s_nop 0
	v_add_u32_e32 v238, s96, v238
	v_mov_b32_e32 v222, v198
	v_ashrrev_i32_e32 v223, 31, v222
	v_lshlrev_b64 v[222:223], 11, v[222:223]
	v_lshl_add_u64 v[222:223], v[222:223], 0, v[196:197]
	v_lshl_add_u64 v[222:223], v[222:223], 2, s[40:41]
	s_add_i32 m0, s96, -16
	s_nop 0
	global_load_lds_dwordx4 v[222:223], off offset:16
	s_add_i32 m0, s96, 1024
	s_nop 0
	global_load_lds_dwordx4 v[222:223], off
	s_add_i32 m0, s96, 1520
	s_nop 0
	global_load_lds_dwordx4 v[222:223], off offset:528
	s_add_i32 m0, s96, 2560
	s_nop 0
	global_load_lds_dwordx4 v[222:223], off offset:512
	v_or_b32_e32 v222, 16, v198
	v_ashrrev_i32_e32 v223, 31, v222
	v_lshlrev_b64 v[222:223], 11, v[222:223]
	v_lshl_add_u64 v[222:223], v[222:223], 0, v[196:197]
	v_lshl_add_u64 v[222:223], v[222:223], 2, s[40:41]
	s_add_i32 m0, s96, 4080
	s_nop 0
	global_load_lds_dwordx4 v[222:223], off offset:16
	s_add_i32 m0, s96, 5120
	s_nop 0
	global_load_lds_dwordx4 v[222:223], off
	s_add_i32 m0, s96, 5616
	s_nop 0
	global_load_lds_dwordx4 v[222:223], off offset:528
	s_add_i32 m0, s96, 6656
	s_nop 0
	global_load_lds_dwordx4 v[222:223], off offset:512
	v_or_b32_e32 v222, 32, v198
	v_ashrrev_i32_e32 v223, 31, v222
	v_lshlrev_b64 v[222:223], 11, v[222:223]
	v_lshl_add_u64 v[222:223], v[222:223], 0, v[196:197]
	v_lshl_add_u64 v[222:223], v[222:223], 2, s[40:41]
	s_add_i32 m0, s96, 8176
	s_nop 0
	global_load_lds_dwordx4 v[222:223], off offset:16
	s_add_i32 m0, s96, 9216
	s_nop 0
	global_load_lds_dwordx4 v[222:223], off
	s_add_i32 m0, s96, 9712
	s_nop 0
	global_load_lds_dwordx4 v[222:223], off offset:528
	s_add_i32 m0, s96, 10752
	s_nop 0
	global_load_lds_dwordx4 v[222:223], off offset:512
	v_or_b32_e32 v222, 48, v198
	v_ashrrev_i32_e32 v223, 31, v222
	v_lshlrev_b64 v[222:223], 11, v[222:223]
	v_lshl_add_u64 v[222:223], v[222:223], 0, v[196:197]
	v_lshl_add_u64 v[222:223], v[222:223], 2, s[40:41]
	s_add_i32 m0, s96, 12272
	s_nop 0
	global_load_lds_dwordx4 v[222:223], off offset:16
	s_add_i32 m0, s96, 13312
	s_nop 0
	global_load_lds_dwordx4 v[222:223], off
	s_add_i32 m0, s96, 13808
	s_nop 0
	global_load_lds_dwordx4 v[222:223], off offset:528
	s_add_i32 m0, s96, 14848
	s_nop 0
	global_load_lds_dwordx4 v[222:223], off offset:512
	s_waitcnt vmcnt(12)
	ds_read_b128 v[186:189], v238
	ds_read_b128 v[190:193], v238 offset:1024
	ds_read_b128 v[230:233], v238 offset:2048
	ds_read_b128 v[234:237], v238 offset:3072
	s_waitcnt lgkmcnt(0)
	v_add_u32_e32 v222, 0x80, v198
	v_ashrrev_i32_e32 v223, 31, v222
	v_lshlrev_b64 v[222:223], 11, v[222:223]
	v_lshl_add_u64 v[222:223], v[222:223], 0, v[196:197]
	v_lshl_add_u64 v[222:223], v[222:223], 2, s[40:41]
	s_add_i32 m0, s96, -16
	s_nop 0
	global_load_lds_dwordx4 v[222:223], off offset:16
	s_add_i32 m0, s96, 1024
	s_nop 0
	global_load_lds_dwordx4 v[222:223], off
	s_add_i32 m0, s96, 1520
	s_nop 0
	global_load_lds_dwordx4 v[222:223], off offset:528
	s_add_i32 m0, s96, 2560
	s_nop 0
	global_load_lds_dwordx4 v[222:223], off offset:512
	s_mov_b64 s[12:13], 0
	s_branch .LBB0_1192

; __device__ __forceinline__ unsigned pk2(float lo, float hi) { unsigned r; asm("v_cvt_pk_bf16_f32 %0, %1, %2" : "=v"(r) : "v"(lo), "v"(hi)); return r; }
; __device__ __forceinline__ float bflo(unsigned u) { return __uint_as_float(u << 16); }
; __device__ __forceinline__ float bfhi(unsigned u) { return __uint_as_float(u & 0xffff0000u); }
;     __device__ __forceinline__ void fused(AccT& acc, const GUnit& u, int wr, int wc, int fr, int fq, LAS unsigned char* lds, int wid, int lane) const {
;     ...
; #pragma unroll
;             for (int ai = 0; ai < 2; ++ai)
; #pragma unroll
;                 for (int m = 0; m < 4; ++m) {
;                     const size_t ro = (size_t)(u.pm * 256 + ai * 128 + wr * 64 + m * 16 + fr) * DM + col0;
; #pragma unroll
;                     for (int bj = 0; bj < 2; ++bj) {
;                         f32x4 x0, x1;
;                         if (base32) { x0 = *(const f32x4*)(base32 + ro + bj * 128); x1 = *(const f32x4*)(base32 + ro + bj * 128 + 4); }
;                         else { const u32x4 w = *(const u32x4*)(base16 + ro + bj * 128); x0 = (f32x4){bflo(w.x), bfhi(w.x), bflo(w.y), bfhi(w.y)}; x1 = (f32x4){bflo(w.z), bfhi(w.z), bflo(w.w), bfhi(w.w)}; }
;                         const f32x4 v0 = x0 + g[bj][0] * acc[ai][bj][m][0], v1 = x1 + g[bj][1] * acc[ai][bj][m][1];
;                         acc[ai][bj][m][0] = v0; acc[ai][bj][m][1] = v1;
;                         u32x4 o; o.x = pk2(v0[0], v0[1]); o.y = pk2(v0[2], v0[3]); o.z = pk2(v1[0], v1[1]); o.w = pk2(v1[2], v1[3]);
;                         *(u32x4*)(X2 + ro + bj * 128) = o;
;                     }
.LBB0_1192:
	v_readlane_b32 s10, v250, 0
	v_readlane_b32 s11, v250, 1
	s_andn2_b64 vcc, exec, s[12:13]
	s_nop 0
	v_lshl_add_u64 v[202:203], v[204:205], 1, s[10:11]
	s_cbranch_vccnz .LBB0_1194
	v_readfirstlane_b32 s96, v0
	v_and_b32_e32 v238, 63, v0
	v_lshlrev_b32_e32 v238, 4, v238
	s_nop 1
	s_lshr_b32 s96, s96, 6
	s_mul_i32 s96, s96, 16384
	s_addk_i32 s96, 1024
	s_nop 0
	v_add_u32_e32 v238, s96, v238
	v_mov_b32_e32 v222, v198
	v_ashrrev_i32_e32 v223, 31, v222
	v_lshlrev_b64 v[222:223], 11, v[222:223]
	v_lshl_add_u64 v[222:223], v[222:223], 0, v[196:197]
	v_lshl_add_u64 v[222:223], v[222:223], 1, s[10:11]
	s_add_i32 m0, s96, 0
	s_nop 0
	global_load_lds_dwordx4 v[222:223], off
	s_add_i32 m0, s96, 768
	s_nop 0
	global_load_lds_dwordx4 v[222:223], off offset:256
	v_or_b32_e32 v222, 16, v198
	v_ashrrev_i32_e32 v223, 31, v222
	v_lshlrev_b64 v[222:223], 11, v[222:223]
	v_lshl_add_u64 v[222:223], v[222:223], 0, v[196:197]
	v_lshl_add_u64 v[222:223], v[222:223], 1, s[10:11]
	s_add_i32 m0, s96, 2048
	s_nop 0
	global_load_lds_dwordx4 v[222:223], off
	s_add_i32 m0, s96, 2816
	s_nop 0
	global_load_lds_dwordx4 v[222:223], off offset:256
	v_or_b32_e32 v222, 32, v198
	v_ashrrev_i32_e32 v223, 31, v222
	v_lshlrev_b64 v[222:223], 11, v[222:223]
	v_lshl_add_u64 v[222:223], v[222:223], 0, v[196:197]
	v_lshl_add_u64 v[222:223], v[222:223], 1, s[10:11]
	s_add_i32 m0, s96, 4096
	s_nop 0
	global_load_lds_dwordx4 v[222:223], off
	s_add_i32 m0, s96, 4864
	s_nop 0
	global_load_lds_dwordx4 v[222:223], off offset:256
	v_or_b32_e32 v222, 48, v198
	v_ashrrev_i32_e32 v223, 31, v222
	v_lshlrev_b64 v[222:223], 11, v[222:223]
	v_lshl_add_u64 v[222:223], v[222:223], 0, v[196:197]
	v_lshl_add_u64 v[222:223], v[222:223], 1, s[10:11]
	s_add_i32 m0, s96, 6144
	s_nop 0
	global_load_lds_dwordx4 v[222:223], off
	s_add_i32 m0, s96, 6912
	s_nop 0
	global_load_lds_dwordx4 v[222:223], off offset:256
	v_add_u32_e32 v222, 0x80, v198
	v_ashrrev_i32_e32 v223, 31, v222
	v_lshlrev_b64 v[222:223], 11, v[222:223]
	v_lshl_add_u64 v[222:223], v[222:223], 0, v[196:197]
	v_lshl_add_u64 v[222:223], v[222:223], 1, s[10:11]
	s_add_i32 m0, s96, 8192
	s_nop 0
	global_load_lds_dwordx4 v[222:223], off
	s_add_i32 m0, s96, 8960
	s_nop 0
	global_load_lds_dwordx4 v[222:223], off offset:256
	v_add_u32_e32 v222, 0x90, v198
	v_ashrrev_i32_e32 v223, 31, v222
	v_lshlrev_b64 v[222:223], 11, v[222:223]
	v_lshl_add_u64 v[222:223], v[222:223], 0, v[196:197]
	v_lshl_add_u64 v[222:223], v[222:223], 1, s[10:11]
	s_add_i32 m0, s96, 10240
	s_nop 0
	global_load_lds_dwordx4 v[222:223], off
	s_add_i32 m0, s96, 11008
	s_nop 0
	global_load_lds_dwordx4 v[222:223], off offset:256
	v_add_u32_e32 v222, 0xa0, v198
	v_ashrrev_i32_e32 v223, 31, v222
	v_lshlrev_b64 v[222:223], 11, v[222:223]
	v_lshl_add_u64 v[222:223], v[222:223], 0, v[196:197]
	v_lshl_add_u64 v[222:223], v[222:223], 1, s[10:11]
	s_add_i32 m0, s96, 12288
	s_nop 0
	global_load_lds_dwordx4 v[222:223], off
	s_add_i32 m0, s96, 13056
	s_nop 0
	global_load_lds_dwordx4 v[222:223], off offset:256
	v_add_u32_e32 v222, 0xb0, v198
	v_ashrrev_i32_e32 v223, 31, v222
	v_lshlrev_b64 v[222:223], 11, v[222:223]
	v_lshl_add_u64 v[222:223], v[222:223], 0, v[196:197]
	v_lshl_add_u64 v[222:223], v[222:223], 1, s[10:11]
	s_add_i32 m0, s96, 14336
	s_nop 0
	global_load_lds_dwordx4 v[222:223], off
	s_add_i32 m0, s96, 15104
	s_nop 0
	global_load_lds_dwordx4 v[222:223], off offset:256
	s_waitcnt vmcnt(14)
	ds_read_b128 v[186:189], v238
	ds_read_b128 v[230:233], v238 offset:1024
	s_waitcnt lgkmcnt(0)
	v_lshlrev_b32_e32 v190, 16, v186
	v_and_b32_e32 v191, 0xffff0000, v186
	v_lshlrev_b32_e32 v192, 16, v187
	v_and_b32_e32 v193, 0xffff0000, v187
	v_lshlrev_b32_e32 v186, 16, v188
	v_and_b32_e32 v187, 0xffff0000, v188
	v_lshlrev_b32_e32 v188, 16, v189
	v_and_b32_e32 v189, 0xffff0000, v189
.LBB0_1194:
	v_readlane_b32 s10, v249, 62
	v_readlane_b32 s11, v249, 63
	v_pk_fma_f32 v[192:193], v[184:185], v[136:137], v[192:193]
	v_pk_fma_f32 v[190:191], v[182:183], v[134:135], v[190:191]
	v_pk_fma_f32 v[188:189], v[180:181], v[132:133], v[188:189]
	v_pk_fma_f32 v[186:187], v[178:179], v[130:131], v[186:187]
	v_lshl_add_u64 v[204:205], v[204:205], 1, s[10:11]
	s_and_b64 vcc, exec, s[34:35]
	v_cvt_pk_bf16_f32 v178, v190, v191
	v_cvt_pk_bf16_f32 v179, v192, v193
	v_cvt_pk_bf16_f32 v180, v186, v187
	v_cvt_pk_bf16_f32 v181, v188, v189
	global_store_dwordx4 v[204:205], v[178:181], off
	s_cbranch_vccnz .LBB0_1199
	s_nop 1
	v_mov_b32_e32 v178, v230
	v_mov_b32_e32 v179, v231
	v_mov_b32_e32 v180, v232
	v_mov_b32_e32 v181, v233
	v_mov_b32_e32 v182, v234
	v_mov_b32_e32 v183, v235
	v_mov_b32_e32 v184, v236
	v_mov_b32_e32 v185, v237
	s_cbranch_execnz .LBB0_1197
.LBB0_1196:
	v_lshlrev_b32_e32 v182, 16, v230
	v_and_b32_e32 v183, 0xffff0000, v230
	v_lshlrev_b32_e32 v184, 16, v231
	v_and_b32_e32 v185, 0xffff0000, v231
	v_lshlrev_b32_e32 v178, 16, v232
	v_and_b32_e32 v179, 0xffff0000, v232
	v_lshlrev_b32_e32 v180, 16, v233
	v_and_b32_e32 v181, 0xffff0000, v233
.LBB0_1197:
	v_pk_fma_f32 v[182:183], v[174:175], v[98:99], v[182:183]
	v_pk_fma_f32 v[178:179], v[170:171], v[78:79], v[178:179]
	v_cvt_pk_bf16_f32 v170, v182, v183
	v_pk_fma_f32 v[184:185], v[176:177], v[100:101], v[184:185]
	v_pk_fma_f32 v[180:181], v[172:173], v[80:81], v[180:181]
	v_cvt_pk_bf16_f32 v171, v184, v185
	v_cvt_pk_bf16_f32 v172, v178, v179
	s_and_b64 vcc, exec, s[34:35]
	v_cvt_pk_bf16_f32 v173, v180, v181
	global_store_dwordx4 v[204:205], v[170:173], off offset:256
	s_nop 1
	v_or_b32_e32 v170, 16, v198
	v_ashrrev_i32_e32 v171, 31, v170
	v_lshlrev_b64 v[170:171], 11, v[170:171]
	v_lshl_add_u64 v[204:205], v[170:171], 0, v[196:197]
	v_lshl_add_u64 v[200:201], v[204:205], 2, s[40:41]
	s_cbranch_vccnz .LBB0_1200
	s_waitcnt vmcnt(14)
	ds_read_b128 v[170:173], v238 offset:4096
	ds_read_b128 v[174:177], v238 offset:5120
	ds_read_b128 v[230:233], v238 offset:6144
	ds_read_b128 v[234:237], v238 offset:7168
	s_waitcnt lgkmcnt(0)
	v_add_u32_e32 v222, 0x90, v198
	v_ashrrev_i32_e32 v223, 31, v222
	v_lshlrev_b64 v[222:223], 11, v[222:223]
	v_lshl_add_u64 v[222:223], v[222:223], 0, v[196:197]
	v_lshl_add_u64 v[222:223], v[222:223], 2, s[40:41]
	s_add_i32 m0, s96, 4080
	s_nop 0
	global_load_lds_dwordx4 v[222:223], off offset:16
	s_add_i32 m0, s96, 5120
	s_nop 0
	global_load_lds_dwordx4 v[222:223], off
	s_add_i32 m0, s96, 5616
	s_nop 0
	global_load_lds_dwordx4 v[222:223], off offset:528
	s_add_i32 m0, s96, 6656
	s_nop 0
	global_load_lds_dwordx4 v[222:223], off offset:512
	s_mov_b64 s[12:13], 0
	s_branch .LBB0_1201

; __device__ __forceinline__ unsigned pk2(float lo, float hi) { unsigned r; asm("v_cvt_pk_bf16_f32 %0, %1, %2" : "=v"(r) : "v"(lo), "v"(hi)); return r; }
; __device__ __forceinline__ float bflo(unsigned u) { return __uint_as_float(u << 16); }
; __device__ __forceinline__ float bfhi(unsigned u) { return __uint_as_float(u & 0xffff0000u); }
;     __device__ __forceinline__ void fused(AccT& acc, const GUnit& u, int wr, int wc, int fr, int fq, LAS unsigned char* lds, int wid, int lane) const {
;     ...
; #pragma unroll
;             for (int ai = 0; ai < 2; ++ai)
; #pragma unroll
;                 for (int m = 0; m < 4; ++m) {
;                     const size_t ro = (size_t)(u.pm * 256 + ai * 128 + wr * 64 + m * 16 + fr) * DM + col0;
; #pragma unroll
;                     for (int bj = 0; bj < 2; ++bj) {
;                         f32x4 x0, x1;
;                         if (base32) { x0 = *(const f32x4*)(base32 + ro + bj * 128); x1 = *(const f32x4*)(base32 + ro + bj * 128 + 4); }
;                         else { const u32x4 w = *(const u32x4*)(base16 + ro + bj * 128); x0 = (f32x4){bflo(w.x), bfhi(w.x), bflo(w.y), bfhi(w.y)}; x1 = (f32x4){bflo(w.z), bfhi(w.z), bflo(w.w), bfhi(w.w)}; }
;                         const f32x4 v0 = x0 + g[bj][0] * acc[ai][bj][m][0], v1 = x1 + g[bj][1] * acc[ai][bj][m][1];
;                         acc[ai][bj][m][0] = v0; acc[ai][bj][m][1] = v1;
;                         u32x4 o; o.x = pk2(v0[0], v0[1]); o.y = pk2(v0[2], v0[3]); o.z = pk2(v1[0], v1[1]); o.w = pk2(v1[2], v1[3]);
;                         *(u32x4*)(X2 + ro + bj * 128) = o;
;                     }
.LBB0_1201:
	v_readlane_b32 s10, v250, 0
	v_readlane_b32 s11, v250, 1
	s_andn2_b64 vcc, exec, s[12:13]
	s_nop 0
	v_lshl_add_u64 v[202:203], v[204:205], 1, s[10:11]
	s_cbranch_vccnz .LBB0_1203
	s_waitcnt vmcnt(14)
	ds_read_b128 v[170:173], v238 offset:2048
	ds_read_b128 v[230:233], v238 offset:3072
	s_waitcnt lgkmcnt(0)
	v_lshlrev_b32_e32 v174, 16, v170
	v_and_b32_e32 v175, 0xffff0000, v170
	v_lshlrev_b32_e32 v176, 16, v171
	v_and_b32_e32 v177, 0xffff0000, v171
	v_lshlrev_b32_e32 v170, 16, v172
	v_and_b32_e32 v171, 0xffff0000, v172
	v_lshlrev_b32_e32 v172, 16, v173
	v_and_b32_e32 v173, 0xffff0000, v173
.LBB0_1203:
	v_readlane_b32 s10, v249, 62
	v_readlane_b32 s11, v249, 63
	v_pk_fma_f32 v[176:177], v[168:169], v[136:137], v[176:177]
	v_pk_fma_f32 v[174:175], v[166:167], v[134:135], v[174:175]
	v_pk_fma_f32 v[172:173], v[164:165], v[132:133], v[172:173]
	v_pk_fma_f32 v[170:171], v[162:163], v[130:131], v[170:171]
	v_lshl_add_u64 v[204:205], v[204:205], 1, s[10:11]
	s_and_b64 vcc, exec, s[34:35]
	v_cvt_pk_bf16_f32 v162, v174, v175
	v_cvt_pk_bf16_f32 v163, v176, v177
	v_cvt_pk_bf16_f32 v164, v170, v171
	v_cvt_pk_bf16_f32 v165, v172, v173
	global_store_dwordx4 v[204:205], v[162:165], off
	s_cbranch_vccnz .LBB0_1208
	s_nop 1
	v_mov_b32_e32 v162, v230
	v_mov_b32_e32 v163, v231
	v_mov_b32_e32 v164, v232
	v_mov_b32_e32 v165, v233
	v_mov_b32_e32 v166, v234
	v_mov_b32_e32 v167, v235
	v_mov_b32_e32 v168, v236
	v_mov_b32_e32 v169, v237
	s_cbranch_execnz .LBB0_1206
.LBB0_1205:
	v_lshlrev_b32_e32 v166, 16, v230
	v_and_b32_e32 v167, 0xffff0000, v230
	v_lshlrev_b32_e32 v168, 16, v231
	v_and_b32_e32 v169, 0xffff0000, v231
	v_lshlrev_b32_e32 v162, 16, v232
	v_and_b32_e32 v163, 0xffff0000, v232
	v_lshlrev_b32_e32 v164, 16, v233
	v_and_b32_e32 v165, 0xffff0000, v233
.LBB0_1206:
	v_pk_fma_f32 v[166:167], v[158:159], v[98:99], v[166:167]
	v_pk_fma_f32 v[162:163], v[154:155], v[78:79], v[162:163]
	v_cvt_pk_bf16_f32 v154, v166, v167
	v_pk_fma_f32 v[168:169], v[160:161], v[100:101], v[168:169]
	v_pk_fma_f32 v[164:165], v[156:157], v[80:81], v[164:165]
	v_cvt_pk_bf16_f32 v155, v168, v169
	v_cvt_pk_bf16_f32 v156, v162, v163
	s_and_b64 vcc, exec, s[34:35]
	v_cvt_pk_bf16_f32 v157, v164, v165
	global_store_dwordx4 v[204:205], v[154:157], off offset:256
	s_nop 1
	v_or_b32_e32 v154, 32, v198
	v_ashrrev_i32_e32 v155, 31, v154
	v_lshlrev_b64 v[154:155], 11, v[154:155]
	v_lshl_add_u64 v[204:205], v[154:155], 0, v[196:197]
	v_lshl_add_u64 v[200:201], v[204:205], 2, s[40:41]
	s_cbranch_vccnz .LBB0_1209
	s_waitcnt vmcnt(16)
	ds_read_b128 v[154:157], v238 offset:8192
	ds_read_b128 v[158:161], v238 offset:9216
	ds_read_b128 v[230:233], v238 offset:10240
	ds_read_b128 v[234:237], v238 offset:11264
	s_waitcnt lgkmcnt(0)
	v_add_u32_e32 v222, 0xa0, v198
	v_ashrrev_i32_e32 v223, 31, v222
	v_lshlrev_b64 v[222:223], 11, v[222:223]
	v_lshl_add_u64 v[222:223], v[222:223], 0, v[196:197]
	v_lshl_add_u64 v[222:223], v[222:223], 2, s[40:41]
	s_add_i32 m0, s96, 8176
	s_nop 0
	global_load_lds_dwordx4 v[222:223], off offset:16
	s_add_i32 m0, s96, 9216
	s_nop 0
	global_load_lds_dwordx4 v[222:223], off
	s_add_i32 m0, s96, 9712
	s_nop 0
	global_load_lds_dwordx4 v[222:223], off offset:528
	s_add_i32 m0, s96, 10752
	s_nop 0
	global_load_lds_dwordx4 v[222:223], off offset:512
	s_mov_b64 s[12:13], 0
	s_branch .LBB0_1210

; __device__ __forceinline__ unsigned pk2(float lo, float hi) { unsigned r; asm("v_cvt_pk_bf16_f32 %0, %1, %2" : "=v"(r) : "v"(lo), "v"(hi)); return r; }
; __device__ __forceinline__ float bflo(unsigned u) { return __uint_as_float(u << 16); }
; __device__ __forceinline__ float bfhi(unsigned u) { return __uint_as_float(u & 0xffff0000u); }
;     __device__ __forceinline__ void fused(AccT& acc, const GUnit& u, int wr, int wc, int fr, int fq, LAS unsigned char* lds, int wid, int lane) const {
;     ...
; #pragma unroll
;             for (int ai = 0; ai < 2; ++ai)
; #pragma unroll
;                 for (int m = 0; m < 4; ++m) {
;                     const size_t ro = (size_t)(u.pm * 256 + ai * 128 + wr * 64 + m * 16 + fr) * DM + col0;
; #pragma unroll
;                     for (int bj = 0; bj < 2; ++bj) {
;                         f32x4 x0, x1;
;                         if (base32) { x0 = *(const f32x4*)(base32 + ro + bj * 128); x1 = *(const f32x4*)(base32 + ro + bj * 128 + 4); }
;                         else { const u32x4 w = *(const u32x4*)(base16 + ro + bj * 128); x0 = (f32x4){bflo(w.x), bfhi(w.x), bflo(w.y), bfhi(w.y)}; x1 = (f32x4){bflo(w.z), bfhi(w.z), bflo(w.w), bfhi(w.w)}; }
;                         const f32x4 v0 = x0 + g[bj][0] * acc[ai][bj][m][0], v1 = x1 + g[bj][1] * acc[ai][bj][m][1];
;                         acc[ai][bj][m][0] = v0; acc[ai][bj][m][1] = v1;
;                         u32x4 o; o.x = pk2(v0[0], v0[1]); o.y = pk2(v0[2], v0[3]); o.z = pk2(v1[0], v1[1]); o.w = pk2(v1[2], v1[3]);
;                         *(u32x4*)(X2 + ro + bj * 128) = o;
;                     }
.LBB0_1210:
	v_readlane_b32 s10, v250, 0
	v_readlane_b32 s11, v250, 1
	s_andn2_b64 vcc, exec, s[12:13]
	s_nop 0
	v_lshl_add_u64 v[202:203], v[204:205], 1, s[10:11]
	s_cbranch_vccnz .LBB0_1212
	s_waitcnt vmcnt(14)
	ds_read_b128 v[154:157], v238 offset:4096
	ds_read_b128 v[230:233], v238 offset:5120
	s_waitcnt lgkmcnt(0)
	v_lshlrev_b32_e32 v158, 16, v154
	v_and_b32_e32 v159, 0xffff0000, v154
	v_lshlrev_b32_e32 v160, 16, v155
	v_and_b32_e32 v161, 0xffff0000, v155
	v_lshlrev_b32_e32 v154, 16, v156
	v_and_b32_e32 v155, 0xffff0000, v156
	v_lshlrev_b32_e32 v156, 16, v157
	v_and_b32_e32 v157, 0xffff0000, v157
.LBB0_1212:
	v_readlane_b32 s10, v249, 62
	v_readlane_b32 s11, v249, 63
	v_pk_fma_f32 v[160:161], v[152:153], v[136:137], v[160:161]
	v_pk_fma_f32 v[158:159], v[150:151], v[134:135], v[158:159]
	v_pk_fma_f32 v[156:157], v[148:149], v[132:133], v[156:157]
	v_pk_fma_f32 v[154:155], v[146:147], v[130:131], v[154:155]
	v_lshl_add_u64 v[204:205], v[204:205], 1, s[10:11]
	s_and_b64 vcc, exec, s[34:35]
	v_cvt_pk_bf16_f32 v146, v158, v159
	v_cvt_pk_bf16_f32 v147, v160, v161
	v_cvt_pk_bf16_f32 v148, v154, v155
	v_cvt_pk_bf16_f32 v149, v156, v157
	global_store_dwordx4 v[204:205], v[146:149], off
	s_cbranch_vccnz .LBB0_1217
	s_nop 1
	v_mov_b32_e32 v146, v230
	v_mov_b32_e32 v147, v231
	v_mov_b32_e32 v148, v232
	v_mov_b32_e32 v149, v233
	v_mov_b32_e32 v150, v234
	v_mov_b32_e32 v151, v235
	v_mov_b32_e32 v152, v236
	v_mov_b32_e32 v153, v237
	s_cbranch_execnz .LBB0_1215
.LBB0_1214:
	v_lshlrev_b32_e32 v150, 16, v230
	v_and_b32_e32 v151, 0xffff0000, v230
	v_lshlrev_b32_e32 v152, 16, v231
	v_and_b32_e32 v153, 0xffff0000, v231
	v_lshlrev_b32_e32 v146, 16, v232
	v_and_b32_e32 v147, 0xffff0000, v232
	v_lshlrev_b32_e32 v148, 16, v233
	v_and_b32_e32 v149, 0xffff0000, v233
.LBB0_1215:
	v_pk_fma_f32 v[150:151], v[142:143], v[98:99], v[150:151]
	v_pk_fma_f32 v[146:147], v[138:139], v[78:79], v[146:147]
	v_cvt_pk_bf16_f32 v138, v150, v151
	v_pk_fma_f32 v[152:153], v[144:145], v[100:101], v[152:153]
	v_pk_fma_f32 v[148:149], v[140:141], v[80:81], v[148:149]
	v_cvt_pk_bf16_f32 v139, v152, v153
	v_cvt_pk_bf16_f32 v140, v146, v147
	s_and_b64 vcc, exec, s[34:35]
	v_cvt_pk_bf16_f32 v141, v148, v149
	global_store_dwordx4 v[204:205], v[138:141], off offset:256
	s_nop 1
	v_or_b32_e32 v138, 48, v198
	v_ashrrev_i32_e32 v139, 31, v138
	v_lshlrev_b64 v[138:139], 11, v[138:139]
	v_lshl_add_u64 v[204:205], v[138:139], 0, v[196:197]
	v_lshl_add_u64 v[200:201], v[204:205], 2, s[40:41]
	s_cbranch_vccnz .LBB0_1218
	s_waitcnt vmcnt(18)
	ds_read_b128 v[138:141], v238 offset:12288
	ds_read_b128 v[142:145], v238 offset:13312
	ds_read_b128 v[230:233], v238 offset:14336
	ds_read_b128 v[234:237], v238 offset:15360
	s_waitcnt lgkmcnt(0)
	v_add_u32_e32 v222, 0xb0, v198
	v_ashrrev_i32_e32 v223, 31, v222
	v_lshlrev_b64 v[222:223], 11, v[222:223]
	v_lshl_add_u64 v[222:223], v[222:223], 0, v[196:197]
	v_lshl_add_u64 v[222:223], v[222:223], 2, s[40:41]
	s_add_i32 m0, s96, 12272
	s_nop 0
	global_load_lds_dwordx4 v[222:223], off offset:16
	s_add_i32 m0, s96, 13312
	s_nop 0
	global_load_lds_dwordx4 v[222:223], off
	s_add_i32 m0, s96, 13808
	s_nop 0
	global_load_lds_dwordx4 v[222:223], off offset:528
	s_add_i32 m0, s96, 14848
	s_nop 0
	global_load_lds_dwordx4 v[222:223], off offset:512
	s_mov_b64 s[12:13], 0
	s_branch .LBB0_1219

; __device__ __forceinline__ unsigned pk2(float lo, float hi) { unsigned r; asm("v_cvt_pk_bf16_f32 %0, %1, %2" : "=v"(r) : "v"(lo), "v"(hi)); return r; }
; __device__ __forceinline__ float bflo(unsigned u) { return __uint_as_float(u << 16); }
; __device__ __forceinline__ float bfhi(unsigned u) { return __uint_as_float(u & 0xffff0000u); }
;     __device__ __forceinline__ void fused(AccT& acc, const GUnit& u, int wr, int wc, int fr, int fq, LAS unsigned char* lds, int wid, int lane) const {
;     ...
; #pragma unroll
;             for (int ai = 0; ai < 2; ++ai)
; #pragma unroll
;                 for (int m = 0; m < 4; ++m) {
;                     const size_t ro = (size_t)(u.pm * 256 + ai * 128 + wr * 64 + m * 16 + fr) * DM + col0;
; #pragma unroll
;                     for (int bj = 0; bj < 2; ++bj) {
;                         f32x4 x0, x1;
;                         if (base32) { x0 = *(const f32x4*)(base32 + ro + bj * 128); x1 = *(const f32x4*)(base32 + ro + bj * 128 + 4); }
;                         else { const u32x4 w = *(const u32x4*)(base16 + ro + bj * 128); x0 = (f32x4){bflo(w.x), bfhi(w.x), bflo(w.y), bfhi(w.y)}; x1 = (f32x4){bflo(w.z), bfhi(w.z), bflo(w.w), bfhi(w.w)}; }
;                         const f32x4 v0 = x0 + g[bj][0] * acc[ai][bj][m][0], v1 = x1 + g[bj][1] * acc[ai][bj][m][1];
;                         acc[ai][bj][m][0] = v0; acc[ai][bj][m][1] = v1;
;                         u32x4 o; o.x = pk2(v0[0], v0[1]); o.y = pk2(v0[2], v0[3]); o.z = pk2(v1[0], v1[1]); o.w = pk2(v1[2], v1[3]);
;                         *(u32x4*)(X2 + ro + bj * 128) = o;
;                     }
.LBB0_1219:
	v_readlane_b32 s10, v250, 0
	v_readlane_b32 s11, v250, 1
	s_andn2_b64 vcc, exec, s[12:13]
	s_nop 0
	v_lshl_add_u64 v[202:203], v[204:205], 1, s[10:11]
	s_cbranch_vccnz .LBB0_1221
	s_waitcnt vmcnt(14)
	ds_read_b128 v[138:141], v238 offset:6144
	ds_read_b128 v[230:233], v238 offset:7168
	s_waitcnt lgkmcnt(0)
	v_lshlrev_b32_e32 v142, 16, v138
	v_and_b32_e32 v143, 0xffff0000, v138
	v_lshlrev_b32_e32 v144, 16, v139
	v_and_b32_e32 v145, 0xffff0000, v139
	v_lshlrev_b32_e32 v138, 16, v140
	v_and_b32_e32 v139, 0xffff0000, v140
	v_lshlrev_b32_e32 v140, 16, v141
	v_and_b32_e32 v141, 0xffff0000, v141
.LBB0_1221:
	v_readlane_b32 s10, v249, 62
	v_readlane_b32 s11, v249, 63
	v_pk_fma_f32 v[144:145], v[128:129], v[136:137], v[144:145]
	v_pk_fma_f32 v[142:143], v[126:127], v[134:135], v[142:143]
	v_pk_fma_f32 v[140:141], v[124:125], v[132:133], v[140:141]
	v_pk_fma_f32 v[138:139], v[122:123], v[130:131], v[138:139]
	v_lshl_add_u64 v[204:205], v[204:205], 1, s[10:11]
	s_and_b64 vcc, exec, s[34:35]
	v_cvt_pk_bf16_f32 v122, v142, v143
	v_cvt_pk_bf16_f32 v123, v144, v145
	v_cvt_pk_bf16_f32 v124, v138, v139
	v_cvt_pk_bf16_f32 v125, v140, v141
	global_store_dwordx4 v[204:205], v[122:125], off
	s_cbranch_vccnz .LBB0_1226
	s_nop 1
	v_mov_b32_e32 v122, v230
	v_mov_b32_e32 v123, v231
	v_mov_b32_e32 v124, v232
	v_mov_b32_e32 v125, v233
	v_mov_b32_e32 v126, v234
	v_mov_b32_e32 v127, v235
	v_mov_b32_e32 v128, v236
	v_mov_b32_e32 v129, v237
	s_cbranch_execnz .LBB0_1224
.LBB0_1223:
	v_lshlrev_b32_e32 v126, 16, v230
	v_and_b32_e32 v127, 0xffff0000, v230
	v_lshlrev_b32_e32 v128, 16, v231
	v_and_b32_e32 v129, 0xffff0000, v231
	v_lshlrev_b32_e32 v122, 16, v232
	v_and_b32_e32 v123, 0xffff0000, v232
	v_lshlrev_b32_e32 v124, 16, v233
	v_and_b32_e32 v125, 0xffff0000, v233
.LBB0_1224:
	v_pk_fma_f32 v[126:127], v[86:87], v[98:99], v[126:127]
	v_pk_fma_f32 v[122:123], v[74:75], v[78:79], v[122:123]
	v_cvt_pk_bf16_f32 v74, v126, v127
	v_pk_fma_f32 v[128:129], v[88:89], v[100:101], v[128:129]
	v_pk_fma_f32 v[124:125], v[76:77], v[80:81], v[124:125]
	v_cvt_pk_bf16_f32 v75, v128, v129
	v_cvt_pk_bf16_f32 v76, v122, v123
	s_and_b64 vcc, exec, s[34:35]
	v_cvt_pk_bf16_f32 v77, v124, v125
	global_store_dwordx4 v[204:205], v[74:77], off offset:256
	s_nop 1
	v_add_u32_e32 v74, 0x80, v198
	v_ashrrev_i32_e32 v75, 31, v74
	v_lshlrev_b64 v[74:75], 11, v[74:75]
	v_lshl_add_u64 v[204:205], v[74:75], 0, v[196:197]
	v_lshl_add_u64 v[200:201], v[204:205], 2, s[40:41]
	s_cbranch_vccnz .LBB0_1227
	s_waitcnt vmcnt(20)
	ds_read_b128 v[74:77], v238
	ds_read_b128 v[86:89], v238 offset:1024
	ds_read_b128 v[230:233], v238 offset:2048
	ds_read_b128 v[234:237], v238 offset:3072
	s_waitcnt lgkmcnt(0)
	s_mov_b64 s[12:13], 0
	s_branch .LBB0_1228

; __device__ __forceinline__ unsigned pk2(float lo, float hi) { unsigned r; asm("v_cvt_pk_bf16_f32 %0, %1, %2" : "=v"(r) : "v"(lo), "v"(hi)); return r; }
; __device__ __forceinline__ float bflo(unsigned u) { return __uint_as_float(u << 16); }
; __device__ __forceinline__ float bfhi(unsigned u) { return __uint_as_float(u & 0xffff0000u); }
;     __device__ __forceinline__ void fused(AccT& acc, const GUnit& u, int wr, int wc, int fr, int fq, LAS unsigned char* lds, int wid, int lane) const {
;     ...
; #pragma unroll
;             for (int ai = 0; ai < 2; ++ai)
; #pragma unroll
;                 for (int m = 0; m < 4; ++m) {
;                     const size_t ro = (size_t)(u.pm * 256 + ai * 128 + wr * 64 + m * 16 + fr) * DM + col0;
; #pragma unroll
;                     for (int bj = 0; bj < 2; ++bj) {
;                         f32x4 x0, x1;
;                         if (base32) { x0 = *(const f32x4*)(base32 + ro + bj * 128); x1 = *(const f32x4*)(base32 + ro + bj * 128 + 4); }
;                         else { const u32x4 w = *(const u32x4*)(base16 + ro + bj * 128); x0 = (f32x4){bflo(w.x), bfhi(w.x), bflo(w.y), bfhi(w.y)}; x1 = (f32x4){bflo(w.z), bfhi(w.z), bflo(w.w), bfhi(w.w)}; }
;                         const f32x4 v0 = x0 + g[bj][0] * acc[ai][bj][m][0], v1 = x1 + g[bj][1] * acc[ai][bj][m][1];
;                         acc[ai][bj][m][0] = v0; acc[ai][bj][m][1] = v1;
;                         u32x4 o; o.x = pk2(v0[0], v0[1]); o.y = pk2(v0[2], v0[3]); o.z = pk2(v1[0], v1[1]); o.w = pk2(v1[2], v1[3]);
;                         *(u32x4*)(X2 + ro + bj * 128) = o;
;                     }
.LBB0_1228:
	v_readlane_b32 s10, v250, 0
	v_readlane_b32 s11, v250, 1
	s_andn2_b64 vcc, exec, s[12:13]
	s_nop 0
	v_lshl_add_u64 v[202:203], v[204:205], 1, s[10:11]
	s_cbranch_vccnz .LBB0_1230
	s_waitcnt vmcnt(14)
	ds_read_b128 v[74:77], v238 offset:8192
	ds_read_b128 v[230:233], v238 offset:9216
	s_waitcnt lgkmcnt(0)
	v_lshlrev_b32_e32 v86, 16, v74
	v_and_b32_e32 v87, 0xffff0000, v74
	v_lshlrev_b32_e32 v88, 16, v75
	v_and_b32_e32 v89, 0xffff0000, v75
	v_lshlrev_b32_e32 v74, 16, v76
	v_and_b32_e32 v75, 0xffff0000, v76
	v_lshlrev_b32_e32 v76, 16, v77
	v_and_b32_e32 v77, 0xffff0000, v77
.LBB0_1230:
	v_readlane_b32 s10, v249, 62
	v_readlane_b32 s11, v249, 63
	v_pk_fma_f32 v[88:89], v[72:73], v[136:137], v[88:89]
	v_pk_fma_f32 v[86:87], v[70:71], v[134:135], v[86:87]
	v_pk_fma_f32 v[76:77], v[68:69], v[132:133], v[76:77]
	v_pk_fma_f32 v[74:75], v[66:67], v[130:131], v[74:75]
	v_lshl_add_u64 v[204:205], v[204:205], 1, s[10:11]
	s_and_b64 vcc, exec, s[34:35]
	v_cvt_pk_bf16_f32 v66, v86, v87
	v_cvt_pk_bf16_f32 v67, v88, v89
	v_cvt_pk_bf16_f32 v68, v74, v75
	v_cvt_pk_bf16_f32 v69, v76, v77
	global_store_dwordx4 v[204:205], v[66:69], off
	s_cbranch_vccnz .LBB0_1235
	s_nop 1
	v_mov_b32_e32 v66, v230
	v_mov_b32_e32 v67, v231
	v_mov_b32_e32 v68, v232
	v_mov_b32_e32 v69, v233
	v_mov_b32_e32 v70, v234
	v_mov_b32_e32 v71, v235
	v_mov_b32_e32 v72, v236
	v_mov_b32_e32 v73, v237
	s_cbranch_execnz .LBB0_1233
.LBB0_1232:
	v_lshlrev_b32_e32 v70, 16, v230
	v_and_b32_e32 v71, 0xffff0000, v230
	v_lshlrev_b32_e32 v72, 16, v231
	v_and_b32_e32 v73, 0xffff0000, v231
	v_lshlrev_b32_e32 v66, 16, v232
	v_and_b32_e32 v67, 0xffff0000, v232
	v_lshlrev_b32_e32 v68, 16, v233
	v_and_b32_e32 v69, 0xffff0000, v233
.LBB0_1233:
	v_pk_fma_f32 v[70:71], v[62:63], v[98:99], v[70:71]
	v_pk_fma_f32 v[66:67], v[58:59], v[78:79], v[66:67]
	v_cvt_pk_bf16_f32 v58, v70, v71
	v_pk_fma_f32 v[72:73], v[64:65], v[100:101], v[72:73]
	v_pk_fma_f32 v[68:69], v[60:61], v[80:81], v[68:69]
	v_cvt_pk_bf16_f32 v59, v72, v73
	v_cvt_pk_bf16_f32 v60, v66, v67
	s_and_b64 vcc, exec, s[34:35]
	v_cvt_pk_bf16_f32 v61, v68, v69
	global_store_dwordx4 v[204:205], v[58:61], off offset:256
	s_nop 1
	v_add_u32_e32 v58, 0x90, v198
	v_ashrrev_i32_e32 v59, 31, v58
	v_lshlrev_b64 v[58:59], 11, v[58:59]
	v_lshl_add_u64 v[204:205], v[58:59], 0, v[196:197]
	v_lshl_add_u64 v[200:201], v[204:205], 2, s[40:41]
	s_cbranch_vccnz .LBB0_1236
	s_waitcnt vmcnt(16)
	ds_read_b128 v[58:61], v238 offset:4096
	ds_read_b128 v[62:65], v238 offset:5120
	ds_read_b128 v[230:233], v238 offset:6144
	ds_read_b128 v[234:237], v238 offset:7168
	s_waitcnt lgkmcnt(0)
	s_mov_b64 s[12:13], 0
	s_branch .LBB0_1237

; __device__ __forceinline__ unsigned pk2(float lo, float hi) { unsigned r; asm("v_cvt_pk_bf16_f32 %0, %1, %2" : "=v"(r) : "v"(lo), "v"(hi)); return r; }
; __device__ __forceinline__ float bflo(unsigned u) { return __uint_as_float(u << 16); }
; __device__ __forceinline__ float bfhi(unsigned u) { return __uint_as_float(u & 0xffff0000u); }
;     __device__ __forceinline__ void fused(AccT& acc, const GUnit& u, int wr, int wc, int fr, int fq, LAS unsigned char* lds, int wid, int lane) const {
;     ...
; #pragma unroll
;             for (int ai = 0; ai < 2; ++ai)
; #pragma unroll
;                 for (int m = 0; m < 4; ++m) {
;                     const size_t ro = (size_t)(u.pm * 256 + ai * 128 + wr * 64 + m * 16 + fr) * DM + col0;
; #pragma unroll
;                     for (int bj = 0; bj < 2; ++bj) {
;                         f32x4 x0, x1;
;                         if (base32) { x0 = *(const f32x4*)(base32 + ro + bj * 128); x1 = *(const f32x4*)(base32 + ro + bj * 128 + 4); }
;                         else { const u32x4 w = *(const u32x4*)(base16 + ro + bj * 128); x0 = (f32x4){bflo(w.x), bfhi(w.x), bflo(w.y), bfhi(w.y)}; x1 = (f32x4){bflo(w.z), bfhi(w.z), bflo(w.w), bfhi(w.w)}; }
;                         const f32x4 v0 = x0 + g[bj][0] * acc[ai][bj][m][0], v1 = x1 + g[bj][1] * acc[ai][bj][m][1];
;                         acc[ai][bj][m][0] = v0; acc[ai][bj][m][1] = v1;
;                         u32x4 o; o.x = pk2(v0[0], v0[1]); o.y = pk2(v0[2], v0[3]); o.z = pk2(v1[0], v1[1]); o.w = pk2(v1[2], v1[3]);
;                         *(u32x4*)(X2 + ro + bj * 128) = o;
;                     }
.LBB0_1237:
	v_readlane_b32 s10, v250, 0
	v_readlane_b32 s11, v250, 1
	s_andn2_b64 vcc, exec, s[12:13]
	s_nop 0
	v_lshl_add_u64 v[202:203], v[204:205], 1, s[10:11]
	s_cbranch_vccnz .LBB0_1239
	s_waitcnt vmcnt(14)
	ds_read_b128 v[58:61], v238 offset:10240
	ds_read_b128 v[230:233], v238 offset:11264
	s_waitcnt lgkmcnt(0)
	v_lshlrev_b32_e32 v62, 16, v58
	v_and_b32_e32 v63, 0xffff0000, v58
	v_lshlrev_b32_e32 v64, 16, v59
	v_and_b32_e32 v65, 0xffff0000, v59
	v_lshlrev_b32_e32 v58, 16, v60
	v_and_b32_e32 v59, 0xffff0000, v60
	v_lshlrev_b32_e32 v60, 16, v61
	v_and_b32_e32 v61, 0xffff0000, v61
.LBB0_1239:
	v_readlane_b32 s10, v249, 62
	v_readlane_b32 s11, v249, 63
	v_pk_fma_f32 v[64:65], v[56:57], v[136:137], v[64:65]
	v_pk_fma_f32 v[62:63], v[54:55], v[134:135], v[62:63]
	v_pk_fma_f32 v[60:61], v[48:49], v[132:133], v[60:61]
	v_pk_fma_f32 v[58:59], v[46:47], v[130:131], v[58:59]
	v_lshl_add_u64 v[204:205], v[204:205], 1, s[10:11]
	s_and_b64 vcc, exec, s[34:35]
	v_cvt_pk_bf16_f32 v46, v62, v63
	v_cvt_pk_bf16_f32 v47, v64, v65
	v_cvt_pk_bf16_f32 v48, v58, v59
	v_cvt_pk_bf16_f32 v49, v60, v61
	global_store_dwordx4 v[204:205], v[46:49], off
	s_cbranch_vccnz .LBB0_1244
	s_nop 1
	v_mov_b32_e32 v46, v230
	v_mov_b32_e32 v47, v231
	v_mov_b32_e32 v48, v232
	v_mov_b32_e32 v49, v233
	v_mov_b32_e32 v54, v234
	v_mov_b32_e32 v55, v235
	v_mov_b32_e32 v56, v236
	v_mov_b32_e32 v57, v237
	s_cbranch_execnz .LBB0_1242
.LBB0_1241:
	v_lshlrev_b32_e32 v54, 16, v230
	v_and_b32_e32 v55, 0xffff0000, v230
	v_lshlrev_b32_e32 v56, 16, v231
	v_and_b32_e32 v57, 0xffff0000, v231
	v_lshlrev_b32_e32 v46, 16, v232
	v_and_b32_e32 v47, 0xffff0000, v232
	v_lshlrev_b32_e32 v48, 16, v233
	v_and_b32_e32 v49, 0xffff0000, v233
.LBB0_1242:
	v_pk_fma_f32 v[52:53], v[52:53], v[100:101], v[56:57]
	v_pk_fma_f32 v[50:51], v[50:51], v[98:99], v[54:55]
	v_pk_fma_f32 v[56:57], v[42:43], v[78:79], v[46:47]
	v_cvt_pk_bf16_f32 v42, v50, v51
	v_pk_fma_f32 v[54:55], v[44:45], v[80:81], v[48:49]
	v_cvt_pk_bf16_f32 v43, v52, v53
	v_cvt_pk_bf16_f32 v44, v56, v57
	s_and_b64 vcc, exec, s[34:35]
	v_cvt_pk_bf16_f32 v45, v54, v55
	global_store_dwordx4 v[204:205], v[42:45], off offset:256
	s_nop 1
	v_add_u32_e32 v42, 0xa0, v198
	v_ashrrev_i32_e32 v43, 31, v42
	v_lshlrev_b64 v[42:43], 11, v[42:43]
	v_lshl_add_u64 v[204:205], v[42:43], 0, v[196:197]
	v_lshl_add_u64 v[200:201], v[204:205], 2, s[40:41]
	s_cbranch_vccnz .LBB0_1245
	s_waitcnt vmcnt(12)
	ds_read_b128 v[42:45], v238 offset:8192
	ds_read_b128 v[46:49], v238 offset:9216
	ds_read_b128 v[230:233], v238 offset:10240
	ds_read_b128 v[234:237], v238 offset:11264
	s_waitcnt lgkmcnt(0)
	s_mov_b64 s[12:13], 0
	s_branch .LBB0_1246

; __device__ __forceinline__ unsigned pk2(float lo, float hi) { unsigned r; asm("v_cvt_pk_bf16_f32 %0, %1, %2" : "=v"(r) : "v"(lo), "v"(hi)); return r; }
; __device__ __forceinline__ float bflo(unsigned u) { return __uint_as_float(u << 16); }
; __device__ __forceinline__ float bfhi(unsigned u) { return __uint_as_float(u & 0xffff0000u); }
;     __device__ __forceinline__ void fused(AccT& acc, const GUnit& u, int wr, int wc, int fr, int fq, LAS unsigned char* lds, int wid, int lane) const {
;     ...
; #pragma unroll
;             for (int ai = 0; ai < 2; ++ai)
; #pragma unroll
;                 for (int m = 0; m < 4; ++m) {
;                     const size_t ro = (size_t)(u.pm * 256 + ai * 128 + wr * 64 + m * 16 + fr) * DM + col0;
; #pragma unroll
;                     for (int bj = 0; bj < 2; ++bj) {
;                         f32x4 x0, x1;
;                         if (base32) { x0 = *(const f32x4*)(base32 + ro + bj * 128); x1 = *(const f32x4*)(base32 + ro + bj * 128 + 4); }
;                         else { const u32x4 w = *(const u32x4*)(base16 + ro + bj * 128); x0 = (f32x4){bflo(w.x), bfhi(w.x), bflo(w.y), bfhi(w.y)}; x1 = (f32x4){bflo(w.z), bfhi(w.z), bflo(w.w), bfhi(w.w)}; }
;                         const f32x4 v0 = x0 + g[bj][0] * acc[ai][bj][m][0], v1 = x1 + g[bj][1] * acc[ai][bj][m][1];
;                         acc[ai][bj][m][0] = v0; acc[ai][bj][m][1] = v1;
;                         u32x4 o; o.x = pk2(v0[0], v0[1]); o.y = pk2(v0[2], v0[3]); o.z = pk2(v1[0], v1[1]); o.w = pk2(v1[2], v1[3]);
;                         *(u32x4*)(X2 + ro + bj * 128) = o;
;                     }
.LBB0_1246:
	v_readlane_b32 s10, v250, 0
	v_readlane_b32 s11, v250, 1
	s_andn2_b64 vcc, exec, s[12:13]
	s_nop 0
	v_lshl_add_u64 v[202:203], v[204:205], 1, s[10:11]
	s_cbranch_vccnz .LBB0_1248
	s_waitcnt vmcnt(14)
	ds_read_b128 v[42:45], v238 offset:12288
	ds_read_b128 v[230:233], v238 offset:13312
	s_waitcnt lgkmcnt(0)
	v_lshlrev_b32_e32 v46, 16, v42
	v_and_b32_e32 v47, 0xffff0000, v42
	v_lshlrev_b32_e32 v48, 16, v43
	v_and_b32_e32 v49, 0xffff0000, v43
	v_lshlrev_b32_e32 v42, 16, v44
	v_and_b32_e32 v43, 0xffff0000, v44
	v_lshlrev_b32_e32 v44, 16, v45
	v_and_b32_e32 v45, 0xffff0000, v45
.LBB0_1248:
	v_readlane_b32 s10, v249, 62
	v_readlane_b32 s11, v249, 63
	v_pk_fma_f32 v[48:49], v[36:37], v[136:137], v[48:49]
	v_pk_fma_f32 v[46:47], v[34:35], v[134:135], v[46:47]
	v_pk_fma_f32 v[44:45], v[28:29], v[132:133], v[44:45]
	v_pk_fma_f32 v[42:43], v[26:27], v[130:131], v[42:43]
	v_lshl_add_u64 v[204:205], v[204:205], 1, s[10:11]
	s_and_b64 vcc, exec, s[34:35]
	v_cvt_pk_bf16_f32 v26, v46, v47
	v_cvt_pk_bf16_f32 v27, v48, v49
	v_cvt_pk_bf16_f32 v28, v42, v43
	v_cvt_pk_bf16_f32 v29, v44, v45
	global_store_dwordx4 v[204:205], v[26:29], off
	s_cbranch_vccnz .LBB0_1253
	s_nop 1
	v_mov_b32_e32 v26, v230
	v_mov_b32_e32 v27, v231
	v_mov_b32_e32 v28, v232
	v_mov_b32_e32 v29, v233
	v_mov_b32_e32 v34, v234
	v_mov_b32_e32 v35, v235
	v_mov_b32_e32 v36, v236
	v_mov_b32_e32 v37, v237
	s_cbranch_execnz .LBB0_1251
.LBB0_1250:
	v_lshlrev_b32_e32 v34, 16, v230
	v_and_b32_e32 v35, 0xffff0000, v230
	v_lshlrev_b32_e32 v36, 16, v231
	v_and_b32_e32 v37, 0xffff0000, v231
	v_lshlrev_b32_e32 v26, 16, v232
	v_and_b32_e32 v27, 0xffff0000, v232
	v_lshlrev_b32_e32 v28, 16, v233
	v_and_b32_e32 v29, 0xffff0000, v233
.LBB0_1251:
	v_pk_fma_f32 v[36:37], v[40:41], v[100:101], v[36:37]
	v_pk_fma_f32 v[34:35], v[38:39], v[98:99], v[34:35]
	v_pk_fma_f32 v[40:41], v[30:31], v[78:79], v[26:27]
	v_cvt_pk_bf16_f32 v26, v34, v35
	v_pk_fma_f32 v[38:39], v[32:33], v[80:81], v[28:29]
	v_cvt_pk_bf16_f32 v27, v36, v37
	v_cvt_pk_bf16_f32 v28, v40, v41
	s_and_b64 vcc, exec, s[34:35]
	v_cvt_pk_bf16_f32 v29, v38, v39
	global_store_dwordx4 v[204:205], v[26:29], off offset:256
	s_nop 1
	v_add_u32_e32 v26, 0xb0, v198
	v_ashrrev_i32_e32 v27, 31, v26
	v_lshlrev_b64 v[26:27], 11, v[26:27]
	v_lshl_add_u64 v[202:203], v[26:27], 0, v[196:197]
	v_lshl_add_u64 v[198:199], v[202:203], 2, s[40:41]
	s_cbranch_vccnz .LBB0_1254
	s_waitcnt vmcnt(8)
	ds_read_b128 v[26:29], v238 offset:12288
	ds_read_b128 v[30:33], v238 offset:13312
	ds_read_b128 v[230:233], v238 offset:14336
	ds_read_b128 v[234:237], v238 offset:15360
	s_waitcnt lgkmcnt(0)
	s_mov_b64 s[12:13], 0
	s_branch .LBB0_1255

;     __device__ __forceinline__ void fused(AccT& acc, const GUnit& u, int wr, int wc, int fr, int fq, LAS unsigned char* lds, int wid, int lane) const {
;     ...
; #pragma unroll
;             for (int ai = 0; ai < 2; ++ai)
; #pragma unroll
;                 for (int m = 0; m < 4; ++m) {
;                     const size_t ro = (size_t)(u.pm * 256 + ai * 128 + wr * 64 + m * 16 + fr) * DM + col0;
; #pragma unroll
;                     for (int bj = 0; bj < 2; ++bj) {
;                         f32x4 x0, x1;
;                         if (base32) { x0 = *(const f32x4*)(base32 + ro + bj * 128); x1 = *(const f32x4*)(base32 + ro + bj * 128 + 4); }
;                         else { const u32x4 w = *(const u32x4*)(base16 + ro + bj * 128); x0 = (f32x4){bflo(w.x), bfhi(w.x), bflo(w.y), bfhi(w.y)}; x1 = (f32x4){bflo(w.z), bfhi(w.z), bflo(w.w), bfhi(w.w)}; }
;                         const f32x4 v0 = x0 + g[bj][0] * acc[ai][bj][m][0], v1 = x1 + g[bj][1] * acc[ai][bj][m][1];
;                         acc[ai][bj][m][0] = v0; acc[ai][bj][m][1] = v1;
;                         u32x4 o; o.x = pk2(v0[0], v0[1]); o.y = pk2(v0[2], v0[3]); o.z = pk2(v1[0], v1[1]); o.w = pk2(v1[2], v1[3]);
;                         *(u32x4*)(X2 + ro + bj * 128) = o;
;                     }
;                     asm volatile("" ::: "memory");
;                 }
;         }
;         {
; #pragma unroll
;             for (int ai = 0; ai < 2; ++ai)
; #pragma unroll
;                 for (int m = 0; m < 4; ++m) {
;                     const int rowl = ai * 128 + wr * 64 + m * 16;
;                     float sq = 0.f; f32x4 lg = (f32x4){0.f, 0.f, 0.f, 0.f};
; #pragma unroll
;                     for (int bj = 0; bj < 2; ++bj) {
;                         const f32x4 x0 = acc[ai][bj][m][0], x1 = acc[ai][bj][m][1];
;                         sq += (x0[0] * x0[0] + x0[1] * x0[1]) + (x0[2] * x0[2] + x0[3] * x0[3]) + (x1[0] * x1[0] + x1[1] * x1[1]) + (x1[2] * x1[2] + x1[3] * x1[3]);
;                         const f32x4 h0 = x0 * G[bj][0], h1 = x1 * G[bj][1];
;                         lg = __builtin_amdgcn_mfma_f32_16x16x32_bf16(pack8(h0[0], h0[1], h0[2], h0[3], h1[0], h1[1], h1[2], h1[3]), wf[bj], lg, 0, 0, 0);
;                     }
;                     sq += __shfl_xor(sq, 16); sq += __shfl_xor(sq, 32);
;                     if (fq == 0) P[(rowl + fr) * 4 + wc] = sq;
.LBB0_1255:
	v_readlane_b32 s10, v250, 0
	v_readlane_b32 s11, v250, 1
	s_andn2_b64 vcc, exec, s[12:13]
	s_nop 0
	v_lshl_add_u64 v[200:201], v[202:203], 1, s[10:11]
	s_cbranch_vccnz .LBB0_1257
	s_waitcnt vmcnt(14)
	ds_read_b128 v[26:29], v238 offset:14336
	ds_read_b128 v[230:233], v238 offset:15360
	s_waitcnt lgkmcnt(0)
	v_lshlrev_b32_e32 v30, 16, v26
	v_and_b32_e32 v31, 0xffff0000, v26
	v_lshlrev_b32_e32 v32, 16, v27
	v_and_b32_e32 v33, 0xffff0000, v27
	v_lshlrev_b32_e32 v26, 16, v28
	v_and_b32_e32 v27, 0xffff0000, v28
	v_lshlrev_b32_e32 v28, 16, v29
	v_and_b32_e32 v29, 0xffff0000, v29
.LBB0_1257:
	v_readlane_b32 s10, v249, 62
	v_readlane_b32 s11, v249, 63
	v_pk_fma_f32 v[32:33], v[24:25], v[136:137], v[32:33]
	v_pk_fma_f32 v[30:31], v[22:23], v[134:135], v[30:31]
	v_pk_fma_f32 v[28:29], v[20:21], v[132:133], v[28:29]
	v_pk_fma_f32 v[26:27], v[18:19], v[130:131], v[26:27]
	v_lshl_add_u64 v[130:131], v[202:203], 1, s[10:11]
	s_and_b64 vcc, exec, s[34:35]
	v_cvt_pk_bf16_f32 v18, v30, v31
	v_cvt_pk_bf16_f32 v19, v32, v33
	v_cvt_pk_bf16_f32 v20, v26, v27
	v_cvt_pk_bf16_f32 v21, v28, v29
	global_store_dwordx4 v[130:131], v[18:21], off
	s_cbranch_vccnz .LBB0_1315
	s_nop 1
	v_mov_b32_e32 v18, v230
	v_mov_b32_e32 v19, v231
	v_mov_b32_e32 v20, v232
	v_mov_b32_e32 v21, v233
	v_mov_b32_e32 v22, v234
	v_mov_b32_e32 v23, v235
	v_mov_b32_e32 v24, v236
	v_mov_b32_e32 v25, v237
	s_cbranch_execnz .LBB0_1260
.LBB0_1259:
	v_lshlrev_b32_e32 v22, 16, v230
	v_and_b32_e32 v23, 0xffff0000, v230
	v_lshlrev_b32_e32 v24, 16, v231
	v_and_b32_e32 v25, 0xffff0000, v231
	v_lshlrev_b32_e32 v18, 16, v232
	v_and_b32_e32 v19, 0xffff0000, v232
	v_lshlrev_b32_e32 v20, 16, v233
	v_and_b32_e32 v21, 0xffff0000, v233
.LBB0_1260:
	v_pk_fma_f32 v[24:25], v[16:17], v[100:101], v[24:25]
	v_pk_fma_f32 v[22:23], v[14:15], v[98:99], v[22:23]
	v_pk_fma_f32 v[18:19], v[10:11], v[78:79], v[18:19]
	v_cvt_pk_bf16_f32 v10, v22, v23
	v_cvt_pk_bf16_f32 v11, v24, v25
	v_pk_fma_f32 v[20:21], v[12:13], v[80:81], v[20:21]
	v_cvt_pk_bf16_f32 v12, v18, v19
	v_pk_add_f32 v[120:121], v[120:121], 1.0 op_sel_hi:[1,0]
	v_cvt_pk_bf16_f32 v13, v20, v21
	global_store_dwordx4 v[130:131], v[10:13], off offset:256
	s_barrier
	v_pk_add_f32 v[118:119], v[118:119], 1.0 op_sel_hi:[1,0]
	v_pk_mul_f32 v[116:117], v[116:117], v[120:121]
	v_mul_f32_e32 v10, v191, v191
	v_mul_f32_e32 v11, v193, v193
	v_fmac_f32_e32 v10, v190, v190
	v_fmac_f32_e32 v11, v192, v192
	v_add_f32_e32 v10, v10, v11
	v_mul_f32_e32 v11, v187, v187
	v_fmac_f32_e32 v11, v186, v186
	v_pk_mul_f32 v[114:115], v[114:115], v[118:119]
	v_pk_add_f32 v[118:119], v[106:107], 1.0 op_sel_hi:[1,0]
	v_pk_add_f32 v[106:107], v[108:109], 1.0 op_sel_hi:[1,0]
	v_add_f32_e32 v10, v11, v10
	v_mul_f32_e32 v11, v189, v189
	v_pk_mul_f32 v[106:107], v[96:97], v[106:107]
	v_pk_mul_f32 v[108:109], v[94:95], v[118:119]
	v_pk_add_f32 v[90:91], v[90:91], 1.0 op_sel_hi:[1,0]
	v_fmac_f32_e32 v11, v188, v188
	v_pk_mul_f32 v[14:15], v[116:117], v[192:193]
	v_pk_mul_f32 v[82:83], v[82:83], v[90:91]
	v_add_f32_e32 v90, v11, v10
	v_pk_mul_f32 v[16:17], v[114:115], v[190:191]
	v_pk_mul_f32 v[78:79], v[106:107], v[188:189]
	v_pk_mul_f32 v[80:81], v[108:109], v[186:187]
	v_cmp_lt_i32_e64 s[34:35], v216, v213
	v_cvt_pk_bf16_f32 v10, v16, v17
	v_cvt_pk_bf16_f32 v11, v14, v15
	v_cvt_pk_bf16_f32 v12, v80, v81
	v_cvt_pk_bf16_f32 v13, v78, v79
	s_nop 1
	v_mul_f32_e32 v14, v183, v183
	v_mul_f32_e32 v15, v185, v185
	v_fmac_f32_e32 v14, v182, v182
	v_fmac_f32_e32 v15, v184, v184
	v_add_f32_e32 v14, v14, v15
	v_mul_f32_e32 v15, v179, v179
	v_fmac_f32_e32 v15, v178, v178
	v_add_f32_e32 v14, v15, v14
	v_mul_f32_e32 v15, v181, v181
	v_fmac_f32_e32 v15, v180, v180
	v_add_f32_e32 v14, v15, v14
	v_add_f32_e32 v15, v90, v14
	v_cndmask_b32_e64 v14, v212, v216, s[34:35]
	v_pk_add_f32 v[94:95], v[112:113], 1.0 op_sel_hi:[1,0]
	v_lshlrev_b32_e32 v14, 2, v14
	v_pk_add_f32 v[96:97], v[110:111], 1.0 op_sel_hi:[1,0]
	v_pk_mul_f32 v[94:95], v[104:105], v[94:95]
	v_pk_add_f32 v[92:93], v[92:93], 1.0 op_sel_hi:[1,0]
	v_mov_b32_e32 v100, v15
	s_nop 1
	v_permlane16_swap_b32_e32 v15, v100
	v_pk_mul_f32 v[96:97], v[102:103], v[96:97]
	v_pk_mul_f32 v[84:85], v[84:85], v[92:93]
	v_pk_mul_f32 v[16:17], v[94:95], v[184:185]
	v_pk_mul_f32 v[90:91], v[96:97], v[182:183]
	v_pk_mul_f32 v[92:93], v[84:85], v[180:181]
	v_pk_mul_f32 v[98:99], v[82:83], v[178:179]
	v_mfma_f32_16x16x32_bf16 v[10:13], v[10:13], v[6:9], 0
	v_cvt_pk_bf16_f32 v78, v90, v91
	v_cvt_pk_bf16_f32 v79, v16, v17
	v_cvt_pk_bf16_f32 v80, v98, v99
	v_cvt_pk_bf16_f32 v81, v92, v93
	s_nop 1
	v_xor_b32_e32 v16, 32, v212
	v_cmp_lt_i32_e64 s[34:35], v16, v213
	s_waitcnt lgkmcnt(0)
	v_add_f32_e32 v15, v15, v100
	v_mfma_f32_16x16x32_bf16 v[10:13], v[78:81], v[2:5], v[10:13]
	v_cndmask_b32_e64 v16, v212, v16, s[34:35]
	v_lshlrev_b32_e32 v17, 2, v16
	ds_bpermute_b32 v16, v17, v15
	v_and_b32_e32 v132, 63, v207
	s_lshl_b32 s10, s59, 2
	s_add_i32 s10, s10, 0
	v_cmp_gt_u32_e32 vcc, 16, v132
	s_and_saveexec_b64 s[12:13], vcc
	s_cbranch_execz .LBB0_1262
	v_lshl_add_u32 v78, v1, 4, s10
	s_waitcnt lgkmcnt(0)
	v_add_f32_e32 v15, v15, v16
	ds_write_b32 v78, v15
